# speedup vs baseline: 1.0461x; 1.0461x over previous
_Z7gemm_gxPKtS0_PKfPtS3_:
	s_lshl_b32 s4, s2, 2
	s_and_b32 s19, s4, 24
	s_bfe_u32 s20, s2, 0x30004
	s_and_b32 s3, s2, 7
	s_lshr_b32 s18, s2, 4
	s_bfe_u32 s40, s2, 0x10003
	s_or_b32 s30, s19, s20
	s_and_b32 s4, 1, s2
	s_lshr_b32 s5, s2, 7
	s_cmp_eq_u32 s4, 1
	s_cselect_b32 s4, 10, 4
	s_cselect_b32 s21, 6, 0
	s_add_i32 s4, s4, s5
	s_add_i32 s5, s4, 4
	s_cmp_lt_u32 s4, 8
	s_cselect_b32 s33, s4, s5
	s_bitcmp1_b32 s2, 3
	s_cselect_b64 s[16:17], -1, 0
	s_and_b64 s[4:5], s[16:17], exec
	s_cselect_b32 s34, 20, 44
	s_cselect_b32 s35, 44, 0
	s_bfe_u32 s4, s2, 0x30003
	s_lshr_b32 s2, s2, 6
	s_add_i32 s2, s21, s2
	s_or_b32 s36, s19, s4
	s_add_i32 s4, s2, 4
	s_cmp_lt_u32 s2, 8
	s_cselect_b32 s37, s2, s4
	s_lshl_b32 s2, s3, 4
	s_add_i32 s2, s2, s18
	v_lshlrev_b32_e32 v5, 4, v0
	v_and_b32_e32 v2, 32, v0
	s_lshr_b32 s3, s2, 2
	s_bfe_u32 s2, s2, 0x20003
	v_bitop3_b32 v2, v5, v2, 48 bitop3:0x6c
	s_and_b32 s3, s3, 0x7fffff8
	s_or_b32 s39, s2, 8
	s_movk_i32 s2, 0x100
	s_load_dwordx8 s[8:15], s[0:1], 0x0
	s_load_dwordx2 s[6:7], s[0:1], 0x20
	v_lshrrev_b32_e32 v1, 8, v0
	v_bfe_u32 v3, v0, 6, 2
	v_and_b32_e32 v4, 15, v0
	v_lshrrev_b32_e32 v6, 2, v0
	v_bfe_u32 v7, v0, 2, 4
	v_and_or_b32 v128, v0, 64, v2
	s_or_b32 s38, s3, s20
	v_and_b32_e32 v8, 48, v0
	v_lshlrev_b32_e32 v9, 6, v0
	v_lshlrev_b32_e32 v10, 2, v0
	v_cmp_gt_u32_e64 s[2:3], s2, v0
	v_and_b32_e32 v11, 8, v0
	v_and_b32_e32 v12, 4, v0
	v_lshlrev_b32_e32 v11, 8, v11
	v_and_b32_e32 v13, 3, v0
	v_lshl_or_b32 v11, v12, 7, v11
	v_lshlrev_b32_e32 v12, 3, v12
	v_lshl_or_b32 v11, v13, 6, v11
	v_and_b32_e32 v13, 48, v0
	v_xor_b32_e32 v12, v12, v13
	v_or_b32_e32 v11, v11, v12
	v_lshrrev_b32_e32 v0, 3, v0
	v_lshlrev_b32_e32 v148, 12, v3
	v_and_b32_e32 v9, 0x3c0, v9
	v_and_b32_e32 v10, 32, v10
	v_lshl_or_b32 v153, v3, 5, v4
	v_and_or_b32 v3, v0, 48, v7
	v_or_b32_e32 v0, 64, v0
	s_movk_i32 s20, 0x70
	v_bitop3_b32 v8, v9, v10, v8 bitop3:0x36
	s_add_i32 s4, 0, 0x10000
	s_add_i32 s5, 0, 0x14000
	s_add_i32 s18, 0, 0x18000
	v_and_or_b32 v0, v0, s20, v7
	v_lshlrev_b32_e32 v158, 13, v1
	v_lshrrev_b32_e32 v2, 1, v128
	v_mov_b32_e32 v129, 0
	v_cmp_eq_u32_e64 s[0:1], 1, v1
	v_lshlrev_b32_e32 v9, 6, v1
	s_add_i32 s19, 0, 0x1c000
	v_lshlrev_b32_e32 v134, 13, v3
	v_lshlrev_b32_e32 v136, 13, v0
	v_or_b32_e32 v0, 0x400, v158
	v_or_b32_e32 v1, 0xc00, v158
	v_or_b32_e32 v3, 0x1400, v158
	v_or_b32_e32 v4, 0x1c00, v158
	v_add_u32_e32 v162, 0, v8
	v_add_u32_e32 v163, 0, v5
	v_add_u32_e32 v173, s4, v5
	v_add_u32_e32 v175, s5, v5
	v_add_u32_e32 v177, s18, v5
	s_mov_b32 s31, 0
	v_add_u32_e32 v149, s4, v11
	s_waitcnt lgkmcnt(0)
	v_lshl_add_u64 v[130:131], s[8:9], 0, v[128:129]
	v_add_u32_e32 v150, s5, v11
	v_lshl_add_u64 v[132:133], s[10:11], 0, v[128:129]
	v_add_u32_e32 v151, s18, v11
	v_add_u32_e32 v152, s19, v11
	v_and_or_b32 v154, v6, 12, v9
	v_mov_b32_e32 v135, v129
	v_mov_b32_e32 v137, v129
	v_or_b32_e32 v155, 0x400, v148
	v_or_b32_e32 v156, 0x100, v148
	v_or_b32_e32 v157, 0x500, v148
	v_or_b32_e32 v159, 0x800, v158
	v_or_b32_e32 v160, 0x1000, v158
	v_or_b32_e32 v161, 0x1800, v158
	s_add_i32 s40, s40, 1
	v_lshlrev_b32_e32 v128, 1, v2
	v_add_u32_e32 v164, 0x2000, v163
	v_add_u32_e32 v165, 0x4000, v163
	v_add_u32_e32 v166, 0x6000, v163
	v_add_u32_e32 v167, 0x8000, v163
	v_add_u32_e32 v168, 0xa000, v163
	v_add_u32_e32 v169, v162, v0
	v_add_u32_e32 v170, v162, v1
	v_add_u32_e32 v171, v162, v3
	v_add_u32_e32 v172, v162, v4
	v_add_u32_e32 v174, 0x2000, v173
	v_add_u32_e32 v176, 0x2000, v175
	v_add_u32_e32 v178, 0x2000, v177
	v_add_u32_e32 v179, s19, v5
	s_branch .LBB1_2

.LBB1_13:
	v_add_u32_e32 v147, v149, v148
	ds_read_b128 v[180:183], v147
	ds_read_b128 v[184:187], v147 offset:1024
	ds_read_b128 v[188:191], v147 offset:256
	ds_read_b128 v[192:195], v147 offset:1280
	s_add_i32 s26, s22, s21
	s_add_i32 s24, s26, 1
	s_ashr_i32 s25, s24, 31
	s_lshl_b64 s[24:25], s[24:25], 7
	v_add_u32_e32 v147, 0xc000, v163
	v_lshl_add_u64 v[196:197], v[138:139], 0, s[24:25]
	v_readfirstlane_b32 s24, v147
	v_add_u32_e32 v147, 0xe000, v163
	v_lshl_add_u64 v[198:199], v[196:197], 0, v[134:135]
	s_mov_b32 m0, s24
	v_readfirstlane_b32 s24, v147
	global_load_lds_dwordx4 v[198:199], off
	v_lshl_add_u64 v[196:197], v[196:197], 0, v[136:137]
	s_mov_b32 m0, s24
	v_add_u32_e32 v147, v162, v158
	global_load_lds_dwordx4 v[196:197], off
	v_add_u32_e32 v248, v162, v159
	v_add_u32_e32 v249, v162, v160
	v_add_u32_e32 v250, v162, v161
	ds_read_b128 v[196:199], v147
	ds_read_b128 v[200:203], v147 offset:1024
	ds_read_b128 v[204:207], v248
	ds_read_b128 v[208:211], v248 offset:1024
	ds_read_b128 v[212:215], v249
	ds_read_b128 v[216:219], v249 offset:1024
	ds_read_b128 v[220:223], v250
	ds_read_b128 v[224:227], v250 offset:1024
	s_waitcnt lgkmcnt(8)
	s_barrier
	s_waitcnt lgkmcnt(0)
	s_setprio 1
	s_waitcnt lgkmcnt(0)
	v_mfma_f32_16x16x32_f16 v[124:127], v[180:183], v[196:199], v[124:127]
	v_mfma_f32_16x16x32_f16 v[120:123], v[188:191], v[196:199], v[120:123]
	v_mfma_f32_16x16x32_f16 v[116:119], v[180:183], v[204:207], v[116:119]
	v_mfma_f32_16x16x32_f16 v[112:115], v[188:191], v[204:207], v[112:115]
	v_mfma_f32_16x16x32_f16 v[108:111], v[180:183], v[212:215], v[108:111]
	v_mfma_f32_16x16x32_f16 v[104:107], v[188:191], v[212:215], v[104:107]
	v_mfma_f32_16x16x32_f16 v[100:103], v[180:183], v[220:223], v[100:103]
	v_mfma_f32_16x16x32_f16 v[96:99], v[188:191], v[220:223], v[96:99]
	v_mfma_f32_16x16x32_f16 v[124:127], v[184:187], v[200:203], v[124:127]
	v_mfma_f32_16x16x32_f16 v[120:123], v[192:195], v[200:203], v[120:123]
	v_mfma_f32_16x16x32_f16 v[116:119], v[184:187], v[208:211], v[116:119]
	v_mfma_f32_16x16x32_f16 v[112:115], v[192:195], v[208:211], v[112:115]
	v_mfma_f32_16x16x32_f16 v[108:111], v[184:187], v[216:219], v[108:111]
	v_mfma_f32_16x16x32_f16 v[104:107], v[192:195], v[216:219], v[104:107]
	v_mfma_f32_16x16x32_f16 v[100:103], v[184:187], v[224:227], v[100:103]
	v_mfma_f32_16x16x32_f16 v[96:99], v[192:195], v[224:227], v[96:99]
	s_setprio 0
	s_barrier
	s_add_i32 s24, s26, 2
	s_ashr_i32 s25, s24, 31
	s_lshl_b64 s[24:25], s[24:25], 7
	v_lshl_add_u64 v[244:245], v[140:141], 0, s[24:25]
	v_readfirstlane_b32 s27, v173
	v_add_u32_e32 v240, v150, v148
	v_lshl_add_u64 v[246:247], v[244:245], 0, v[134:135]
	s_mov_b32 m0, s27
	v_readfirstlane_b32 s27, v174
	ds_read_b128 v[228:231], v240
	ds_read_b128 v[232:235], v240 offset:1024
	ds_read_b128 v[236:239], v240 offset:256
	ds_read_b128 v[240:243], v240 offset:1280
	global_load_lds_dwordx4 v[246:247], off
	v_lshl_add_u64 v[244:245], v[244:245], 0, v[136:137]
	s_mov_b32 m0, s27
	s_add_i32 s21, s21, 2
	global_load_lds_dwordx4 v[244:245], off
	s_barrier
	s_waitcnt lgkmcnt(0)
	s_setprio 1
	s_waitcnt lgkmcnt(0)
	v_mfma_f32_16x16x32_f16 v[92:95], v[228:231], v[196:199], v[92:95]
	v_mfma_f32_16x16x32_f16 v[88:91], v[236:239], v[196:199], v[88:91]
	v_mfma_f32_16x16x32_f16 v[84:87], v[228:231], v[204:207], v[84:87]
	v_mfma_f32_16x16x32_f16 v[80:83], v[236:239], v[204:207], v[80:83]
	v_mfma_f32_16x16x32_f16 v[76:79], v[228:231], v[212:215], v[76:79]
	v_mfma_f32_16x16x32_f16 v[72:75], v[236:239], v[212:215], v[72:75]
	v_mfma_f32_16x16x32_f16 v[68:71], v[228:231], v[220:223], v[68:71]
	v_mfma_f32_16x16x32_f16 v[64:67], v[236:239], v[220:223], v[64:67]
	v_mfma_f32_16x16x32_f16 v[92:95], v[232:235], v[200:203], v[92:95]
	v_mfma_f32_16x16x32_f16 v[88:91], v[240:243], v[200:203], v[88:91]
	v_mfma_f32_16x16x32_f16 v[84:87], v[232:235], v[208:211], v[84:87]
	v_mfma_f32_16x16x32_f16 v[80:83], v[240:243], v[208:211], v[80:83]
	v_mfma_f32_16x16x32_f16 v[76:79], v[232:235], v[216:219], v[76:79]
	v_mfma_f32_16x16x32_f16 v[72:75], v[240:243], v[216:219], v[72:75]
	v_mfma_f32_16x16x32_f16 v[68:71], v[232:235], v[224:227], v[68:71]
	v_mfma_f32_16x16x32_f16 v[64:67], v[240:243], v[224:227], v[64:67]
	s_setprio 0
	v_lshl_add_u64 v[244:245], v[142:143], 0, s[24:25]
	v_readfirstlane_b32 s27, v163
	v_lshl_add_u64 v[246:247], v[244:245], 0, v[134:135]
	s_mov_b32 m0, s27
	v_readfirstlane_b32 s27, v164
	s_barrier
	ds_read_b128 v[196:199], v147 offset:16384
	ds_read_b128 v[200:203], v147 offset:17408
	ds_read_b128 v[204:207], v248 offset:16384
	ds_read_b128 v[208:211], v248 offset:17408
	ds_read_b128 v[212:215], v249 offset:16384
	ds_read_b128 v[216:219], v249 offset:17408
	ds_read_b128 v[220:223], v250 offset:16384
	ds_read_b128 v[224:227], v250 offset:17408
	global_load_lds_dwordx4 v[246:247], off
	v_lshl_add_u64 v[244:245], v[244:245], 0, v[136:137]
	s_mov_b32 m0, s27
	s_nop 0
	global_load_lds_dwordx4 v[244:245], off
	s_barrier
	s_waitcnt lgkmcnt(0)
	s_setprio 1
	s_waitcnt lgkmcnt(0)
	v_mfma_f32_16x16x32_f16 v[60:63], v[180:183], v[196:199], v[60:63]
	v_mfma_f32_16x16x32_f16 v[56:59], v[188:191], v[196:199], v[56:59]
	v_mfma_f32_16x16x32_f16 v[52:55], v[180:183], v[204:207], v[52:55]
	v_mfma_f32_16x16x32_f16 v[48:51], v[188:191], v[204:207], v[48:51]
	v_mfma_f32_16x16x32_f16 v[44:47], v[180:183], v[212:215], v[44:47]
	v_mfma_f32_16x16x32_f16 v[40:43], v[188:191], v[212:215], v[40:43]
	v_mfma_f32_16x16x32_f16 v[36:39], v[180:183], v[220:223], v[36:39]
	v_mfma_f32_16x16x32_f16 v[32:35], v[188:191], v[220:223], v[32:35]
	v_mfma_f32_16x16x32_f16 v[60:63], v[184:187], v[200:203], v[60:63]
	v_mfma_f32_16x16x32_f16 v[56:59], v[192:195], v[200:203], v[56:59]
	v_mfma_f32_16x16x32_f16 v[52:55], v[184:187], v[208:211], v[52:55]
	v_mfma_f32_16x16x32_f16 v[48:51], v[192:195], v[208:211], v[48:51]
	v_mfma_f32_16x16x32_f16 v[44:47], v[184:187], v[216:219], v[44:47]
	v_mfma_f32_16x16x32_f16 v[40:43], v[192:195], v[216:219], v[40:43]
	v_mfma_f32_16x16x32_f16 v[36:39], v[184:187], v[224:227], v[36:39]
	v_mfma_f32_16x16x32_f16 v[32:35], v[192:195], v[224:227], v[32:35]
	s_setprio 0
	s_barrier
	v_lshl_add_u64 v[180:181], v[144:145], 0, s[24:25]
	v_readfirstlane_b32 s27, v175
	v_lshl_add_u64 v[182:183], v[180:181], 0, v[134:135]
	s_mov_b32 m0, s27
	v_readfirstlane_b32 s27, v176
	global_load_lds_dwordx4 v[182:183], off
	v_lshl_add_u64 v[180:181], v[180:181], 0, v[136:137]
	s_mov_b32 m0, s27
	s_nop 0
	global_load_lds_dwordx4 v[180:181], off
	s_waitcnt vmcnt(6)
	s_barrier
	s_setprio 1
	v_mfma_f32_16x16x32_f16 v[28:31], v[228:231], v[196:199], v[28:31]
	v_mfma_f32_16x16x32_f16 v[24:27], v[236:239], v[196:199], v[24:27]
	v_mfma_f32_16x16x32_f16 v[20:23], v[228:231], v[204:207], v[20:23]
	v_mfma_f32_16x16x32_f16 v[16:19], v[236:239], v[204:207], v[16:19]
	v_mfma_f32_16x16x32_f16 v[12:15], v[228:231], v[212:215], v[12:15]
	v_mfma_f32_16x16x32_f16 v[8:11], v[236:239], v[212:215], v[8:11]
	v_mfma_f32_16x16x32_f16 v[4:7], v[228:231], v[220:223], v[4:7]
	v_mfma_f32_16x16x32_f16 v[0:3], v[236:239], v[220:223], v[0:3]
	v_mfma_f32_16x16x32_f16 v[28:31], v[232:235], v[200:203], v[28:31]
	v_mfma_f32_16x16x32_f16 v[24:27], v[240:243], v[200:203], v[24:27]
	v_mfma_f32_16x16x32_f16 v[20:23], v[232:235], v[208:211], v[20:23]
	v_mfma_f32_16x16x32_f16 v[16:19], v[240:243], v[208:211], v[16:19]
	v_mfma_f32_16x16x32_f16 v[12:15], v[232:235], v[216:219], v[12:15]
	v_mfma_f32_16x16x32_f16 v[8:11], v[240:243], v[216:219], v[8:11]
	v_mfma_f32_16x16x32_f16 v[4:7], v[232:235], v[224:227], v[4:7]
	v_mfma_f32_16x16x32_f16 v[0:3], v[240:243], v[224:227], v[0:3]
	s_setprio 0
	v_add_u32_e32 v192, v151, v148
	s_barrier
	ds_read_b128 v[180:183], v192
	ds_read_b128 v[184:187], v192 offset:1024
	ds_read_b128 v[188:191], v192 offset:256
	ds_read_b128 v[192:195], v192 offset:1280
	v_lshl_add_u64 v[228:229], v[138:139], 0, s[24:25]
	v_readfirstlane_b32 s24, v165
	v_lshl_add_u64 v[230:231], v[228:229], 0, v[134:135]
	s_mov_b32 m0, s24
	v_readfirstlane_b32 s24, v166
	ds_read_b128 v[196:199], v147 offset:32768
	ds_read_b128 v[200:203], v147 offset:33792
	ds_read_b128 v[204:207], v248 offset:32768
	ds_read_b128 v[208:211], v248 offset:33792
	ds_read_b128 v[212:215], v249 offset:32768
	ds_read_b128 v[216:219], v249 offset:33792
	ds_read_b128 v[220:223], v250 offset:32768
	ds_read_b128 v[224:227], v250 offset:33792
	global_load_lds_dwordx4 v[230:231], off
	v_lshl_add_u64 v[228:229], v[228:229], 0, v[136:137]
	s_mov_b32 m0, s24
	s_nop 0
	global_load_lds_dwordx4 v[228:229], off
	s_waitcnt lgkmcnt(8)
	s_barrier
	s_waitcnt lgkmcnt(0)
	s_setprio 1
	s_waitcnt lgkmcnt(0)
	v_mfma_f32_16x16x32_f16 v[124:127], v[180:183], v[196:199], v[124:127]
	v_mfma_f32_16x16x32_f16 v[120:123], v[188:191], v[196:199], v[120:123]
	v_mfma_f32_16x16x32_f16 v[116:119], v[180:183], v[204:207], v[116:119]
	v_mfma_f32_16x16x32_f16 v[112:115], v[188:191], v[204:207], v[112:115]
	v_mfma_f32_16x16x32_f16 v[108:111], v[180:183], v[212:215], v[108:111]
	v_mfma_f32_16x16x32_f16 v[104:107], v[188:191], v[212:215], v[104:107]
	v_mfma_f32_16x16x32_f16 v[100:103], v[180:183], v[220:223], v[100:103]
	v_mfma_f32_16x16x32_f16 v[96:99], v[188:191], v[220:223], v[96:99]
	v_mfma_f32_16x16x32_f16 v[124:127], v[184:187], v[200:203], v[124:127]
	v_mfma_f32_16x16x32_f16 v[120:123], v[192:195], v[200:203], v[120:123]
	v_mfma_f32_16x16x32_f16 v[116:119], v[184:187], v[208:211], v[116:119]
	v_mfma_f32_16x16x32_f16 v[112:115], v[192:195], v[208:211], v[112:115]
	v_mfma_f32_16x16x32_f16 v[108:111], v[184:187], v[216:219], v[108:111]
	v_mfma_f32_16x16x32_f16 v[104:107], v[192:195], v[216:219], v[104:107]
	v_mfma_f32_16x16x32_f16 v[100:103], v[184:187], v[224:227], v[100:103]
	v_mfma_f32_16x16x32_f16 v[96:99], v[192:195], v[224:227], v[96:99]
	s_setprio 0
	s_barrier
	s_add_i32 s24, s26, 3
	s_ashr_i32 s25, s24, 31
	s_lshl_b64 s[24:25], s[24:25], 7
	v_lshl_add_u64 v[244:245], v[140:141], 0, s[24:25]
	v_readfirstlane_b32 s26, v177
	v_add_u32_e32 v240, v152, v148
	v_lshl_add_u64 v[246:247], v[244:245], 0, v[134:135]
	s_mov_b32 m0, s26
	v_readfirstlane_b32 s26, v178
	ds_read_b128 v[228:231], v240
	ds_read_b128 v[232:235], v240 offset:1024
	ds_read_b128 v[236:239], v240 offset:256
	ds_read_b128 v[240:243], v240 offset:1280
	global_load_lds_dwordx4 v[246:247], off
	v_lshl_add_u64 v[244:245], v[244:245], 0, v[136:137]
	s_mov_b32 m0, s26
	s_nop 0
	global_load_lds_dwordx4 v[244:245], off
	s_barrier
	s_waitcnt lgkmcnt(0)
	s_setprio 1
	s_waitcnt lgkmcnt(0)
	v_mfma_f32_16x16x32_f16 v[92:95], v[228:231], v[196:199], v[92:95]
	v_mfma_f32_16x16x32_f16 v[88:91], v[236:239], v[196:199], v[88:91]
	v_mfma_f32_16x16x32_f16 v[84:87], v[228:231], v[204:207], v[84:87]
	v_mfma_f32_16x16x32_f16 v[80:83], v[236:239], v[204:207], v[80:83]
	v_mfma_f32_16x16x32_f16 v[76:79], v[228:231], v[212:215], v[76:79]
	v_mfma_f32_16x16x32_f16 v[72:75], v[236:239], v[212:215], v[72:75]
	v_mfma_f32_16x16x32_f16 v[68:71], v[228:231], v[220:223], v[68:71]
	v_mfma_f32_16x16x32_f16 v[64:67], v[236:239], v[220:223], v[64:67]
	v_mfma_f32_16x16x32_f16 v[92:95], v[232:235], v[200:203], v[92:95]
	v_mfma_f32_16x16x32_f16 v[88:91], v[240:243], v[200:203], v[88:91]
	v_mfma_f32_16x16x32_f16 v[84:87], v[232:235], v[208:211], v[84:87]
	v_mfma_f32_16x16x32_f16 v[80:83], v[240:243], v[208:211], v[80:83]
	v_mfma_f32_16x16x32_f16 v[76:79], v[232:235], v[216:219], v[76:79]
	v_mfma_f32_16x16x32_f16 v[72:75], v[240:243], v[216:219], v[72:75]
	v_mfma_f32_16x16x32_f16 v[68:71], v[232:235], v[224:227], v[68:71]
	v_mfma_f32_16x16x32_f16 v[64:67], v[240:243], v[224:227], v[64:67]
	s_setprio 0
	v_lshl_add_u64 v[244:245], v[142:143], 0, s[24:25]
	v_readfirstlane_b32 s26, v167
	v_lshl_add_u64 v[246:247], v[244:245], 0, v[134:135]
	s_mov_b32 m0, s26
	v_readfirstlane_b32 s26, v168
	s_barrier
	ds_read_b128 v[196:199], v147 offset:49152
	ds_read_b128 v[200:203], v147 offset:50176
	ds_read_b128 v[204:207], v248 offset:49152
	ds_read_b128 v[208:211], v248 offset:50176
	ds_read_b128 v[212:215], v249 offset:49152
	ds_read_b128 v[216:219], v249 offset:50176
	ds_read_b128 v[220:223], v250 offset:49152
	ds_read_b128 v[224:227], v250 offset:50176
	global_load_lds_dwordx4 v[246:247], off
	v_lshl_add_u64 v[244:245], v[244:245], 0, v[136:137]
	s_mov_b32 m0, s26
	s_nop 0
	global_load_lds_dwordx4 v[244:245], off
	s_barrier
	s_waitcnt lgkmcnt(0)
	s_setprio 1
	s_waitcnt lgkmcnt(0)
	v_mfma_f32_16x16x32_f16 v[60:63], v[180:183], v[196:199], v[60:63]
	v_mfma_f32_16x16x32_f16 v[56:59], v[188:191], v[196:199], v[56:59]
	v_mfma_f32_16x16x32_f16 v[52:55], v[180:183], v[204:207], v[52:55]
	v_mfma_f32_16x16x32_f16 v[48:51], v[188:191], v[204:207], v[48:51]
	v_mfma_f32_16x16x32_f16 v[44:47], v[180:183], v[212:215], v[44:47]
	v_mfma_f32_16x16x32_f16 v[40:43], v[188:191], v[212:215], v[40:43]
	v_mfma_f32_16x16x32_f16 v[36:39], v[180:183], v[220:223], v[36:39]
	v_mfma_f32_16x16x32_f16 v[32:35], v[188:191], v[220:223], v[32:35]
	v_mfma_f32_16x16x32_f16 v[60:63], v[184:187], v[200:203], v[60:63]
	v_mfma_f32_16x16x32_f16 v[56:59], v[192:195], v[200:203], v[56:59]
	v_mfma_f32_16x16x32_f16 v[52:55], v[184:187], v[208:211], v[52:55]
	v_mfma_f32_16x16x32_f16 v[48:51], v[192:195], v[208:211], v[48:51]
	v_mfma_f32_16x16x32_f16 v[44:47], v[184:187], v[216:219], v[44:47]
	v_mfma_f32_16x16x32_f16 v[40:43], v[192:195], v[216:219], v[40:43]
	v_mfma_f32_16x16x32_f16 v[36:39], v[184:187], v[224:227], v[36:39]
	v_mfma_f32_16x16x32_f16 v[32:35], v[192:195], v[224:227], v[32:35]
	s_setprio 0
	s_barrier
	v_lshl_add_u64 v[180:181], v[144:145], 0, s[24:25]
	v_readfirstlane_b32 s24, v179
	v_lshl_add_u64 v[182:183], v[180:181], 0, v[134:135]
	s_mov_b32 m0, s24
	v_readfirstlane_b32 s24, v146
	global_load_lds_dwordx4 v[182:183], off
	v_lshl_add_u64 v[180:181], v[180:181], 0, v[136:137]
	s_mov_b32 m0, s24
	s_nop 0
	global_load_lds_dwordx4 v[180:181], off
	s_waitcnt vmcnt(6)
	s_barrier
	s_setprio 1
	v_mfma_f32_16x16x32_f16 v[28:31], v[228:231], v[196:199], v[28:31]
	v_mfma_f32_16x16x32_f16 v[24:27], v[236:239], v[196:199], v[24:27]
	v_mfma_f32_16x16x32_f16 v[20:23], v[228:231], v[204:207], v[20:23]
	v_mfma_f32_16x16x32_f16 v[16:19], v[236:239], v[204:207], v[16:19]
	v_mfma_f32_16x16x32_f16 v[12:15], v[228:231], v[212:215], v[12:15]
	v_mfma_f32_16x16x32_f16 v[8:11], v[236:239], v[212:215], v[8:11]
	v_mfma_f32_16x16x32_f16 v[4:7], v[228:231], v[220:223], v[4:7]
	v_mfma_f32_16x16x32_f16 v[0:3], v[236:239], v[220:223], v[0:3]
	v_mfma_f32_16x16x32_f16 v[28:31], v[232:235], v[200:203], v[28:31]
	v_mfma_f32_16x16x32_f16 v[24:27], v[240:243], v[200:203], v[24:27]
	v_mfma_f32_16x16x32_f16 v[20:23], v[232:235], v[208:211], v[20:23]
	v_mfma_f32_16x16x32_f16 v[16:19], v[240:243], v[208:211], v[16:19]
	v_mfma_f32_16x16x32_f16 v[12:15], v[232:235], v[216:219], v[12:15]
	v_mfma_f32_16x16x32_f16 v[8:11], v[240:243], v[216:219], v[8:11]
	v_mfma_f32_16x16x32_f16 v[4:7], v[232:235], v[224:227], v[4:7]
	v_mfma_f32_16x16x32_f16 v[0:3], v[240:243], v[224:227], v[0:3]
	s_setprio 0
	s_cmp_ge_i32 s21, s5
	s_barrier
	s_cbranch_scc0 .LBB1_13
.LBB1_14:
	v_and_b32_e32 v254, 0x60, v153
	v_and_b32_e32 v255, 12, v154
	v_lshl_or_b32 v254, v255, 1, v254
	v_or_b32_e32 v254, s4, v254
	v_lshlrev_b32_e32 v254, 2, v254
	s_and_b64 vcc, exec, s[18:19]
	s_cbranch_vccnz .Lgx_zero_bias
	global_load_dwordx4 v[238:241], v254, s[12:13]
	global_load_dwordx4 v[242:245], v254, s[12:13] offset:16
	global_load_dwordx4 v[246:249], v254, s[12:13] offset:512
	global_load_dwordx4 v[250:253], v254, s[12:13] offset:528
	s_branch .Lgx_bias_done
.Lgx_zero_bias:
	v_mov_b32_e32 v238, 0
	v_mov_b32_e32 v239, 0
	v_mov_b32_e32 v240, 0
	v_mov_b32_e32 v241, 0
	v_mov_b32_e32 v242, 0
	v_mov_b32_e32 v243, 0
	v_mov_b32_e32 v244, 0
	v_mov_b32_e32 v245, 0
	v_mov_b32_e32 v246, 0
	v_mov_b32_e32 v247, 0
	v_mov_b32_e32 v248, 0
	v_mov_b32_e32 v249, 0
	v_mov_b32_e32 v250, 0
	v_mov_b32_e32 v251, 0
	v_mov_b32_e32 v252, 0
	v_mov_b32_e32 v253, 0
.Lgx_bias_done:
	s_add_i32 s5, s22, s41
	s_add_i32 s26, s5, -1
	s_ashr_i32 s27, s26, 31
	s_xor_b64 s[24:25], s[18:19], -1
	s_lshl_b64 s[26:27], s[26:27], 7
	s_add_u32 s22, s23, s26
	v_add_u32_e32 v138, v149, v148
	v_add_u32_e32 v142, v149, v155
	v_add_u32_e32 v146, v149, v156
	v_add_u32_e32 v147, v149, v157
	s_addc_u32 s23, s42, s27
	v_add_u32_e32 v190, 0xc000, v163
	ds_read_b128 v[138:141], v138
	ds_read_b128 v[142:145], v142
	ds_read_b128 v[180:183], v146
	ds_read_b128 v[184:187], v147
	v_lshl_add_u64 v[146:147], s[22:23], 0, v[128:129]
	v_readfirstlane_b32 s5, v190
	v_lshl_add_u64 v[188:189], v[146:147], 0, v[134:135]
	s_mov_b32 m0, s5
	v_lshl_add_u64 v[146:147], v[146:147], 0, v[136:137]
	global_load_lds_dwordx4 v[188:189], off
	v_add_u32_e32 v188, 0xe000, v163
	v_add_u32_e32 v236, v162, v160
	v_readfirstlane_b32 s5, v188
	s_mov_b32 m0, s5
	v_add_u32_e32 v237, v162, v161
	global_load_lds_dwordx4 v[146:147], off
	v_add_u32_e32 v146, v162, v158
	v_add_u32_e32 v147, v162, v159
	ds_read_b128 v[188:191], v146
	ds_read_b128 v[192:195], v169
	ds_read_b128 v[196:199], v147
	ds_read_b128 v[200:203], v170
	ds_read_b128 v[204:207], v236
	ds_read_b128 v[208:211], v171
	ds_read_b128 v[212:215], v237
	ds_read_b128 v[216:219], v172
	s_barrier
	s_waitcnt lgkmcnt(0)
	s_setprio 1
	s_waitcnt lgkmcnt(0)
	v_mfma_f32_16x16x32_f16 v[124:127], v[138:141], v[188:191], v[124:127]
	v_mfma_f32_16x16x32_f16 v[120:123], v[180:183], v[188:191], v[120:123]
	v_mfma_f32_16x16x32_f16 v[116:119], v[138:141], v[196:199], v[116:119]
	v_mfma_f32_16x16x32_f16 v[112:115], v[180:183], v[196:199], v[112:115]
	v_mfma_f32_16x16x32_f16 v[108:111], v[138:141], v[204:207], v[108:111]
	v_mfma_f32_16x16x32_f16 v[104:107], v[180:183], v[204:207], v[104:107]
	v_mfma_f32_16x16x32_f16 v[100:103], v[138:141], v[212:215], v[100:103]
	v_mfma_f32_16x16x32_f16 v[96:99], v[180:183], v[212:215], v[96:99]
	v_mfma_f32_16x16x32_f16 v[124:127], v[142:145], v[192:195], v[124:127]
	v_mfma_f32_16x16x32_f16 v[120:123], v[184:187], v[192:195], v[120:123]
	v_mfma_f32_16x16x32_f16 v[116:119], v[142:145], v[200:203], v[116:119]
	v_mfma_f32_16x16x32_f16 v[112:115], v[184:187], v[200:203], v[112:115]
	v_mfma_f32_16x16x32_f16 v[108:111], v[142:145], v[208:211], v[108:111]
	v_mfma_f32_16x16x32_f16 v[104:107], v[184:187], v[208:211], v[104:107]
	v_mfma_f32_16x16x32_f16 v[100:103], v[142:145], v[216:219], v[100:103]
	v_mfma_f32_16x16x32_f16 v[96:99], v[184:187], v[216:219], v[96:99]
	s_setprio 0
	v_add_u32_e32 v220, v150, v148
	v_add_u32_e32 v224, v150, v155
	v_add_u32_e32 v228, v150, v156
	v_add_u32_e32 v232, v150, v157
	s_barrier
	ds_read_b128 v[220:223], v220
	ds_read_b128 v[224:227], v224
	ds_read_b128 v[228:231], v228
	ds_read_b128 v[232:235], v232
	s_barrier
	s_waitcnt lgkmcnt(0)
	s_setprio 1
	s_waitcnt lgkmcnt(0)
	v_mfma_f32_16x16x32_f16 v[92:95], v[220:223], v[188:191], v[92:95]
	v_mfma_f32_16x16x32_f16 v[88:91], v[228:231], v[188:191], v[88:91]
	v_mfma_f32_16x16x32_f16 v[84:87], v[220:223], v[196:199], v[84:87]
	v_mfma_f32_16x16x32_f16 v[80:83], v[228:231], v[196:199], v[80:83]
	v_mfma_f32_16x16x32_f16 v[76:79], v[220:223], v[204:207], v[76:79]
	v_mfma_f32_16x16x32_f16 v[72:75], v[228:231], v[204:207], v[72:75]
	v_mfma_f32_16x16x32_f16 v[68:71], v[220:223], v[212:215], v[68:71]
	v_mfma_f32_16x16x32_f16 v[64:67], v[228:231], v[212:215], v[64:67]
	v_mfma_f32_16x16x32_f16 v[92:95], v[224:227], v[192:195], v[92:95]
	v_mfma_f32_16x16x32_f16 v[88:91], v[232:235], v[192:195], v[88:91]
	v_mfma_f32_16x16x32_f16 v[84:87], v[224:227], v[200:203], v[84:87]
	v_mfma_f32_16x16x32_f16 v[80:83], v[232:235], v[200:203], v[80:83]
	v_mfma_f32_16x16x32_f16 v[76:79], v[224:227], v[208:211], v[76:79]
	v_mfma_f32_16x16x32_f16 v[72:75], v[232:235], v[208:211], v[72:75]
	v_mfma_f32_16x16x32_f16 v[68:71], v[224:227], v[216:219], v[68:71]
	v_mfma_f32_16x16x32_f16 v[64:67], v[232:235], v[216:219], v[64:67]
	s_setprio 0
	s_barrier
	ds_read_b128 v[188:191], v146 offset:16384
	ds_read_b128 v[192:195], v169 offset:16384
	ds_read_b128 v[196:199], v147 offset:16384
	ds_read_b128 v[200:203], v170 offset:16384
	ds_read_b128 v[204:207], v236 offset:16384
	ds_read_b128 v[208:211], v171 offset:16384
	ds_read_b128 v[212:215], v237 offset:16384
	ds_read_b128 v[216:219], v172 offset:16384
	s_waitcnt vmcnt(4)
	s_barrier
	s_waitcnt lgkmcnt(0)
	s_setprio 1
	s_waitcnt lgkmcnt(0)
	v_mfma_f32_16x16x32_f16 v[60:63], v[138:141], v[188:191], v[60:63]
	v_mfma_f32_16x16x32_f16 v[56:59], v[180:183], v[188:191], v[56:59]
	v_mfma_f32_16x16x32_f16 v[52:55], v[138:141], v[196:199], v[52:55]
	v_mfma_f32_16x16x32_f16 v[48:51], v[180:183], v[196:199], v[48:51]
	v_mfma_f32_16x16x32_f16 v[44:47], v[138:141], v[204:207], v[44:47]
	v_mfma_f32_16x16x32_f16 v[40:43], v[180:183], v[204:207], v[40:43]
	v_mfma_f32_16x16x32_f16 v[36:39], v[138:141], v[212:215], v[36:39]
	v_mfma_f32_16x16x32_f16 v[32:35], v[180:183], v[212:215], v[32:35]
	v_mfma_f32_16x16x32_f16 v[60:63], v[142:145], v[192:195], v[60:63]
	v_mfma_f32_16x16x32_f16 v[56:59], v[184:187], v[192:195], v[56:59]
	v_mfma_f32_16x16x32_f16 v[52:55], v[142:145], v[200:203], v[52:55]
	v_mfma_f32_16x16x32_f16 v[48:51], v[184:187], v[200:203], v[48:51]
	v_mfma_f32_16x16x32_f16 v[44:47], v[142:145], v[208:211], v[44:47]
	v_mfma_f32_16x16x32_f16 v[40:43], v[184:187], v[208:211], v[40:43]
	v_mfma_f32_16x16x32_f16 v[36:39], v[142:145], v[216:219], v[36:39]
	v_mfma_f32_16x16x32_f16 v[32:35], v[184:187], v[216:219], v[32:35]
	s_setprio 0
	s_setprio 1
	v_mfma_f32_16x16x32_f16 v[28:31], v[220:223], v[188:191], v[28:31]
	v_mfma_f32_16x16x32_f16 v[24:27], v[228:231], v[188:191], v[24:27]
	v_mfma_f32_16x16x32_f16 v[20:23], v[220:223], v[196:199], v[20:23]
	v_mfma_f32_16x16x32_f16 v[16:19], v[228:231], v[196:199], v[16:19]
	v_mfma_f32_16x16x32_f16 v[12:15], v[220:223], v[204:207], v[12:15]
	v_mfma_f32_16x16x32_f16 v[8:11], v[228:231], v[204:207], v[8:11]
	v_mfma_f32_16x16x32_f16 v[4:7], v[220:223], v[212:215], v[4:7]
	v_mfma_f32_16x16x32_f16 v[0:3], v[228:231], v[212:215], v[0:3]
	v_mfma_f32_16x16x32_f16 v[28:31], v[224:227], v[192:195], v[28:31]
	v_mfma_f32_16x16x32_f16 v[24:27], v[232:235], v[192:195], v[24:27]
	v_mfma_f32_16x16x32_f16 v[20:23], v[224:227], v[200:203], v[20:23]
	v_mfma_f32_16x16x32_f16 v[16:19], v[232:235], v[200:203], v[16:19]
	v_mfma_f32_16x16x32_f16 v[12:15], v[224:227], v[208:211], v[12:15]
	v_mfma_f32_16x16x32_f16 v[8:11], v[232:235], v[208:211], v[8:11]
	v_mfma_f32_16x16x32_f16 v[4:7], v[224:227], v[216:219], v[4:7]
	v_mfma_f32_16x16x32_f16 v[0:3], v[232:235], v[216:219], v[0:3]
	s_setprio 0
	v_add_u32_e32 v138, v151, v148
	v_add_u32_e32 v142, v151, v155
	v_add_u32_e32 v180, v151, v156
	v_add_u32_e32 v184, v151, v157
	s_barrier
	ds_read_b128 v[138:141], v138
	ds_read_b128 v[142:145], v142
	ds_read_b128 v[180:183], v180
	ds_read_b128 v[184:187], v184
	ds_read_b128 v[188:191], v146 offset:32768
	ds_read_b128 v[192:195], v169 offset:32768
	ds_read_b128 v[196:199], v147 offset:32768
	ds_read_b128 v[200:203], v170 offset:32768
	ds_read_b128 v[204:207], v236 offset:32768
	ds_read_b128 v[208:211], v171 offset:32768
	ds_read_b128 v[212:215], v237 offset:32768
	ds_read_b128 v[216:219], v172 offset:32768
	s_waitcnt vmcnt(2)
	s_barrier
	s_waitcnt lgkmcnt(0)
	s_setprio 1
	s_waitcnt lgkmcnt(0)
	v_mfma_f32_16x16x32_f16 v[124:127], v[138:141], v[188:191], v[124:127]
	v_mfma_f32_16x16x32_f16 v[120:123], v[180:183], v[188:191], v[120:123]
	v_mfma_f32_16x16x32_f16 v[116:119], v[138:141], v[196:199], v[116:119]
	v_mfma_f32_16x16x32_f16 v[112:115], v[180:183], v[196:199], v[112:115]
	v_mfma_f32_16x16x32_f16 v[108:111], v[138:141], v[204:207], v[108:111]
	v_mfma_f32_16x16x32_f16 v[104:107], v[180:183], v[204:207], v[104:107]
	v_mfma_f32_16x16x32_f16 v[100:103], v[138:141], v[212:215], v[100:103]
	v_mfma_f32_16x16x32_f16 v[96:99], v[180:183], v[212:215], v[96:99]
	v_mfma_f32_16x16x32_f16 v[124:127], v[142:145], v[192:195], v[124:127]
	v_mfma_f32_16x16x32_f16 v[120:123], v[184:187], v[192:195], v[120:123]
	v_mfma_f32_16x16x32_f16 v[116:119], v[142:145], v[200:203], v[116:119]
	v_mfma_f32_16x16x32_f16 v[112:115], v[184:187], v[200:203], v[112:115]
	v_mfma_f32_16x16x32_f16 v[108:111], v[142:145], v[208:211], v[108:111]
	v_mfma_f32_16x16x32_f16 v[104:107], v[184:187], v[208:211], v[104:107]
	v_mfma_f32_16x16x32_f16 v[100:103], v[142:145], v[216:219], v[100:103]
	v_mfma_f32_16x16x32_f16 v[96:99], v[184:187], v[216:219], v[96:99]
	s_setprio 0
	v_add_u32_e32 v220, v152, v148
	v_add_u32_e32 v224, v152, v155
	v_add_u32_e32 v228, v152, v156
	v_add_u32_e32 v232, v152, v157
	s_barrier
	ds_read_b128 v[220:223], v220
	ds_read_b128 v[224:227], v224
	ds_read_b128 v[228:231], v228
	ds_read_b128 v[232:235], v232
	s_waitcnt vmcnt(0)
	s_barrier
	s_waitcnt lgkmcnt(0)
	s_setprio 1
	s_waitcnt lgkmcnt(0)
	v_mfma_f32_16x16x32_f16 v[92:95], v[220:223], v[188:191], v[92:95]
	v_mfma_f32_16x16x32_f16 v[88:91], v[228:231], v[188:191], v[88:91]
	v_mfma_f32_16x16x32_f16 v[84:87], v[220:223], v[196:199], v[84:87]
	v_mfma_f32_16x16x32_f16 v[80:83], v[228:231], v[196:199], v[80:83]
	v_mfma_f32_16x16x32_f16 v[76:79], v[220:223], v[204:207], v[76:79]
	v_mfma_f32_16x16x32_f16 v[72:75], v[228:231], v[204:207], v[72:75]
	v_mfma_f32_16x16x32_f16 v[68:71], v[220:223], v[212:215], v[68:71]
	v_mfma_f32_16x16x32_f16 v[64:67], v[228:231], v[212:215], v[64:67]
	v_mfma_f32_16x16x32_f16 v[92:95], v[224:227], v[192:195], v[92:95]
	v_mfma_f32_16x16x32_f16 v[88:91], v[232:235], v[192:195], v[88:91]
	v_mfma_f32_16x16x32_f16 v[84:87], v[224:227], v[200:203], v[84:87]
	v_mfma_f32_16x16x32_f16 v[80:83], v[232:235], v[200:203], v[80:83]
	v_mfma_f32_16x16x32_f16 v[76:79], v[224:227], v[208:211], v[76:79]
	v_mfma_f32_16x16x32_f16 v[72:75], v[232:235], v[208:211], v[72:75]
	v_mfma_f32_16x16x32_f16 v[68:71], v[224:227], v[216:219], v[68:71]
	v_mfma_f32_16x16x32_f16 v[64:67], v[232:235], v[216:219], v[64:67]
	s_setprio 0
	s_barrier
	ds_read_b128 v[188:191], v146 offset:49152
	ds_read_b128 v[192:195], v169 offset:49152
	ds_read_b128 v[196:199], v147 offset:49152
	ds_read_b128 v[200:203], v170 offset:49152
	ds_read_b128 v[204:207], v236 offset:49152
	ds_read_b128 v[208:211], v171 offset:49152
	ds_read_b128 v[212:215], v237 offset:49152
	ds_read_b128 v[216:219], v172 offset:49152
	s_barrier
	s_waitcnt lgkmcnt(0)
	s_setprio 1
	s_waitcnt lgkmcnt(0)
	v_mfma_f32_16x16x32_f16 v[60:63], v[138:141], v[188:191], v[60:63]
	v_mfma_f32_16x16x32_f16 v[56:59], v[180:183], v[188:191], v[56:59]
	v_mfma_f32_16x16x32_f16 v[52:55], v[138:141], v[196:199], v[52:55]
	v_mfma_f32_16x16x32_f16 v[48:51], v[180:183], v[196:199], v[48:51]
	v_mfma_f32_16x16x32_f16 v[44:47], v[138:141], v[204:207], v[44:47]
	v_mfma_f32_16x16x32_f16 v[40:43], v[180:183], v[204:207], v[40:43]
	v_mfma_f32_16x16x32_f16 v[36:39], v[138:141], v[212:215], v[36:39]
	v_mfma_f32_16x16x32_f16 v[32:35], v[180:183], v[212:215], v[32:35]
	v_mfma_f32_16x16x32_f16 v[60:63], v[142:145], v[192:195], v[60:63]
	v_mfma_f32_16x16x32_f16 v[56:59], v[184:187], v[192:195], v[56:59]
	v_mfma_f32_16x16x32_f16 v[52:55], v[142:145], v[200:203], v[52:55]
	v_mfma_f32_16x16x32_f16 v[48:51], v[184:187], v[200:203], v[48:51]
	v_mfma_f32_16x16x32_f16 v[44:47], v[142:145], v[208:211], v[44:47]
	v_mfma_f32_16x16x32_f16 v[40:43], v[184:187], v[208:211], v[40:43]
	v_mfma_f32_16x16x32_f16 v[36:39], v[142:145], v[216:219], v[36:39]
	v_mfma_f32_16x16x32_f16 v[32:35], v[184:187], v[216:219], v[32:35]
	s_setprio 0
	s_setprio 1
	v_mfma_f32_16x16x32_f16 v[28:31], v[220:223], v[188:191], v[28:31]
	v_mfma_f32_16x16x32_f16 v[24:27], v[228:231], v[188:191], v[24:27]
	v_mfma_f32_16x16x32_f16 v[20:23], v[220:223], v[196:199], v[20:23]
	v_mfma_f32_16x16x32_f16 v[16:19], v[228:231], v[196:199], v[16:19]
	v_mfma_f32_16x16x32_f16 v[12:15], v[220:223], v[204:207], v[12:15]
	v_mfma_f32_16x16x32_f16 v[8:11], v[228:231], v[204:207], v[8:11]
	v_mfma_f32_16x16x32_f16 v[4:7], v[220:223], v[212:215], v[4:7]
	v_mfma_f32_16x16x32_f16 v[0:3], v[228:231], v[212:215], v[0:3]
	v_mfma_f32_16x16x32_f16 v[28:31], v[224:227], v[192:195], v[28:31]
	v_mfma_f32_16x16x32_f16 v[24:27], v[232:235], v[192:195], v[24:27]
	v_mfma_f32_16x16x32_f16 v[20:23], v[224:227], v[200:203], v[20:23]
	v_mfma_f32_16x16x32_f16 v[16:19], v[232:235], v[200:203], v[16:19]
	v_mfma_f32_16x16x32_f16 v[12:15], v[224:227], v[208:211], v[12:15]
	v_mfma_f32_16x16x32_f16 v[8:11], v[232:235], v[208:211], v[8:11]
	v_mfma_f32_16x16x32_f16 v[4:7], v[224:227], v[216:219], v[4:7]
	v_mfma_f32_16x16x32_f16 v[0:3], v[232:235], v[216:219], v[0:3]
	s_setprio 0
	s_barrier
	s_and_saveexec_b64 s[22:23], s[2:3]
	s_cbranch_execz .LBB1_16
	s_barrier
.LBB1_16:
	s_or_b64 exec, exec, s[22:23]
	v_and_b32_e32 v180, 0x60, v153
	v_and_b32_e32 v181, 12, v154
	v_lshl_or_b32 v180, v181, 1, v180
	v_or_b32_e32 v180, s4, v180
	v_and_b32_e32 v181, 64, v154
	v_and_b32_e32 v182, 15, v153
	v_or3_b32 v181, v181, v182, s20
	v_lshlrev_b32_e32 v180, 1, v180
	v_lshl_or_b32 v180, v181, 13, v180
	s_and_b64 s[22:23], s[18:19], exec
	s_cselect_b32 s22, s6, s14
	s_cselect_b32 s23, s7, s15
	v_add_u32_e32 v181, 0x20000, v180
	v_add_u32_e32 v182, 0x40000, v180
	v_add_u32_e32 v183, 0x60000, v180
	v_add_u32_e32 v184, 0x100000, v180
	v_add_u32_e32 v185, 0x120000, v180
	v_add_u32_e32 v186, 0x140000, v180
	v_add_u32_e32 v187, 0x160000, v180
	s_waitcnt vmcnt(0)
	v_pk_add_f32 v[124:125], v[124:125], v[238:239]
	v_pk_add_f32 v[126:127], v[126:127], v[240:241]
	v_pk_add_f32 v[120:121], v[120:121], v[242:243]
	v_pk_add_f32 v[122:123], v[122:123], v[244:245]
	v_cvt_pk_f16_f32 v188, v124, v125
	v_cvt_pk_f16_f32 v189, v126, v127
	v_cvt_pk_f16_f32 v190, v120, v121
	v_cvt_pk_f16_f32 v191, v122, v123
	global_store_dwordx4 v180, v[188:191], s[22:23]
	v_pk_add_f32 v[116:117], v[116:117], v[238:239]
	v_pk_add_f32 v[118:119], v[118:119], v[240:241]
	v_pk_add_f32 v[112:113], v[112:113], v[242:243]
	v_pk_add_f32 v[114:115], v[114:115], v[244:245]
	v_cvt_pk_f16_f32 v192, v116, v117
	v_cvt_pk_f16_f32 v193, v118, v119
	v_cvt_pk_f16_f32 v194, v112, v113
	v_cvt_pk_f16_f32 v195, v114, v115
	global_store_dwordx4 v181, v[192:195], s[22:23]
	v_pk_add_f32 v[108:109], v[108:109], v[238:239]
	v_pk_add_f32 v[110:111], v[110:111], v[240:241]
	v_pk_add_f32 v[104:105], v[104:105], v[242:243]
	v_pk_add_f32 v[106:107], v[106:107], v[244:245]
	v_cvt_pk_f16_f32 v196, v108, v109
	v_cvt_pk_f16_f32 v197, v110, v111
	v_cvt_pk_f16_f32 v198, v104, v105
	v_cvt_pk_f16_f32 v199, v106, v107
	global_store_dwordx4 v182, v[196:199], s[22:23]
	v_pk_add_f32 v[100:101], v[100:101], v[238:239]
	v_pk_add_f32 v[102:103], v[102:103], v[240:241]
	v_pk_add_f32 v[96:97], v[96:97], v[242:243]
	v_pk_add_f32 v[98:99], v[98:99], v[244:245]
	v_cvt_pk_f16_f32 v200, v100, v101
	v_cvt_pk_f16_f32 v201, v102, v103
	v_cvt_pk_f16_f32 v202, v96, v97
	v_cvt_pk_f16_f32 v203, v98, v99
	global_store_dwordx4 v183, v[200:203], s[22:23]
	v_pk_add_f32 v[92:93], v[92:93], v[246:247]
	v_pk_add_f32 v[94:95], v[94:95], v[248:249]
	v_pk_add_f32 v[88:89], v[88:89], v[250:251]
	v_pk_add_f32 v[90:91], v[90:91], v[252:253]
	v_cvt_pk_f16_f32 v188, v92, v93
	v_cvt_pk_f16_f32 v189, v94, v95
	v_cvt_pk_f16_f32 v190, v88, v89
	v_cvt_pk_f16_f32 v191, v90, v91
	global_store_dwordx4 v180, v[188:191], s[22:23] offset:256
	v_pk_add_f32 v[84:85], v[84:85], v[246:247]
	v_pk_add_f32 v[86:87], v[86:87], v[248:249]
	v_pk_add_f32 v[80:81], v[80:81], v[250:251]
	v_pk_add_f32 v[82:83], v[82:83], v[252:253]
	v_cvt_pk_f16_f32 v192, v84, v85
	v_cvt_pk_f16_f32 v193, v86, v87
	v_cvt_pk_f16_f32 v194, v80, v81
	v_cvt_pk_f16_f32 v195, v82, v83
	global_store_dwordx4 v181, v[192:195], s[22:23] offset:256
	v_pk_add_f32 v[76:77], v[76:77], v[246:247]
	v_pk_add_f32 v[78:79], v[78:79], v[248:249]
	v_pk_add_f32 v[72:73], v[72:73], v[250:251]
	v_pk_add_f32 v[74:75], v[74:75], v[252:253]
	v_cvt_pk_f16_f32 v196, v76, v77
	v_cvt_pk_f16_f32 v197, v78, v79
	v_cvt_pk_f16_f32 v198, v72, v73
	v_cvt_pk_f16_f32 v199, v74, v75
	global_store_dwordx4 v182, v[196:199], s[22:23] offset:256
	v_pk_add_f32 v[68:69], v[68:69], v[246:247]
	v_pk_add_f32 v[70:71], v[70:71], v[248:249]
	v_pk_add_f32 v[64:65], v[64:65], v[250:251]
	v_pk_add_f32 v[66:67], v[66:67], v[252:253]
	v_cvt_pk_f16_f32 v200, v68, v69
	v_cvt_pk_f16_f32 v201, v70, v71
	v_cvt_pk_f16_f32 v202, v64, v65
	v_cvt_pk_f16_f32 v203, v66, v67
	global_store_dwordx4 v183, v[200:203], s[22:23] offset:256
	v_pk_add_f32 v[60:61], v[60:61], v[238:239]
	v_pk_add_f32 v[62:63], v[62:63], v[240:241]
	v_pk_add_f32 v[56:57], v[56:57], v[242:243]
	v_pk_add_f32 v[58:59], v[58:59], v[244:245]
	v_cvt_pk_f16_f32 v188, v60, v61
	v_cvt_pk_f16_f32 v189, v62, v63
	v_cvt_pk_f16_f32 v190, v56, v57
	v_cvt_pk_f16_f32 v191, v58, v59
	global_store_dwordx4 v184, v[188:191], s[22:23]
	v_pk_add_f32 v[52:53], v[52:53], v[238:239]
	v_pk_add_f32 v[54:55], v[54:55], v[240:241]
	v_pk_add_f32 v[48:49], v[48:49], v[242:243]
	v_pk_add_f32 v[50:51], v[50:51], v[244:245]
	v_cvt_pk_f16_f32 v192, v52, v53
	v_cvt_pk_f16_f32 v193, v54, v55
	v_cvt_pk_f16_f32 v194, v48, v49
	v_cvt_pk_f16_f32 v195, v50, v51
	global_store_dwordx4 v185, v[192:195], s[22:23]
	v_pk_add_f32 v[44:45], v[44:45], v[238:239]
	v_pk_add_f32 v[46:47], v[46:47], v[240:241]
	v_pk_add_f32 v[40:41], v[40:41], v[242:243]
	v_pk_add_f32 v[42:43], v[42:43], v[244:245]
	v_cvt_pk_f16_f32 v196, v44, v45
	v_cvt_pk_f16_f32 v197, v46, v47
	v_cvt_pk_f16_f32 v198, v40, v41
	v_cvt_pk_f16_f32 v199, v42, v43
	global_store_dwordx4 v186, v[196:199], s[22:23]
	v_pk_add_f32 v[36:37], v[36:37], v[238:239]
	v_pk_add_f32 v[38:39], v[38:39], v[240:241]
	v_pk_add_f32 v[32:33], v[32:33], v[242:243]
	v_pk_add_f32 v[34:35], v[34:35], v[244:245]
	v_cvt_pk_f16_f32 v200, v36, v37
	v_cvt_pk_f16_f32 v201, v38, v39
	v_cvt_pk_f16_f32 v202, v32, v33
	v_cvt_pk_f16_f32 v203, v34, v35
	global_store_dwordx4 v187, v[200:203], s[22:23]
	v_pk_add_f32 v[28:29], v[28:29], v[246:247]
	v_pk_add_f32 v[30:31], v[30:31], v[248:249]
	v_pk_add_f32 v[24:25], v[24:25], v[250:251]
	v_pk_add_f32 v[26:27], v[26:27], v[252:253]
	v_cvt_pk_f16_f32 v188, v28, v29
	v_cvt_pk_f16_f32 v189, v30, v31
	v_cvt_pk_f16_f32 v190, v24, v25
	v_cvt_pk_f16_f32 v191, v26, v27
	global_store_dwordx4 v184, v[188:191], s[22:23] offset:256
	v_pk_add_f32 v[20:21], v[20:21], v[246:247]
	v_pk_add_f32 v[22:23], v[22:23], v[248:249]
	v_pk_add_f32 v[16:17], v[16:17], v[250:251]
	v_pk_add_f32 v[18:19], v[18:19], v[252:253]
	v_cvt_pk_f16_f32 v192, v20, v21
	v_cvt_pk_f16_f32 v193, v22, v23
	v_cvt_pk_f16_f32 v194, v16, v17
	v_cvt_pk_f16_f32 v195, v18, v19
	global_store_dwordx4 v185, v[192:195], s[22:23] offset:256
	v_pk_add_f32 v[12:13], v[12:13], v[246:247]
	v_pk_add_f32 v[14:15], v[14:15], v[248:249]
	v_pk_add_f32 v[8:9], v[8:9], v[250:251]
	v_pk_add_f32 v[10:11], v[10:11], v[252:253]
	v_cvt_pk_f16_f32 v196, v12, v13
	v_cvt_pk_f16_f32 v197, v14, v15
	v_cvt_pk_f16_f32 v198, v8, v9
	v_cvt_pk_f16_f32 v199, v10, v11
	global_store_dwordx4 v186, v[196:199], s[22:23] offset:256
	v_pk_add_f32 v[4:5], v[4:5], v[246:247]
	v_pk_add_f32 v[6:7], v[6:7], v[248:249]
	v_pk_add_f32 v[0:1], v[0:1], v[250:251]
	v_pk_add_f32 v[2:3], v[2:3], v[252:253]
	v_cvt_pk_f16_f32 v200, v4, v5
	v_cvt_pk_f16_f32 v201, v6, v7
	v_cvt_pk_f16_f32 v202, v0, v1
	v_cvt_pk_f16_f32 v203, v2, v3
	global_store_dwordx4 v187, v[200:203], s[22:23] offset:256
	s_add_i32 s4, s31, 1
	s_cmp_eq_u32 s31, s40
	s_mov_b32 s31, s4
	s_cbranch_scc0 .LBB1_2

	.amdhsa_kernel _Z7gemm_gxPKtS0_PKfPtS3_
		.amdhsa_group_segment_fixed_size 0
		.amdhsa_private_segment_fixed_size 0
		.amdhsa_kernarg_size 40
		.amdhsa_user_sgpr_count 2
		.amdhsa_user_sgpr_dispatch_ptr 0
		.amdhsa_user_sgpr_queue_ptr 0
		.amdhsa_user_sgpr_kernarg_segment_ptr 1
		.amdhsa_user_sgpr_dispatch_id 0
		.amdhsa_user_sgpr_kernarg_preload_length 0
		.amdhsa_user_sgpr_kernarg_preload_offset 0
		.amdhsa_user_sgpr_private_segment_size 0
		.amdhsa_uses_dynamic_stack 0
		.amdhsa_enable_private_segment 0
		.amdhsa_system_sgpr_workgroup_id_x 1
		.amdhsa_system_sgpr_workgroup_id_y 0
		.amdhsa_system_sgpr_workgroup_id_z 0
		.amdhsa_system_sgpr_workgroup_info 0
		.amdhsa_system_vgpr_workitem_id 0
		.amdhsa_next_free_vgpr 256
		.amdhsa_next_free_sgpr 52
		.amdhsa_accum_offset 256
		.amdhsa_reserve_vcc 1
		.amdhsa_float_round_mode_32 0
		.amdhsa_float_round_mode_16_64 0
		.amdhsa_float_denorm_mode_32 3
		.amdhsa_float_denorm_mode_16_64 3
		.amdhsa_dx10_clamp 1
		.amdhsa_ieee_mode 1
		.amdhsa_fp16_overflow 0
		.amdhsa_tg_split 0
		.amdhsa_exception_fp_ieee_invalid_op 0
		.amdhsa_exception_fp_denorm_src 0
		.amdhsa_exception_fp_ieee_div_zero 0
		.amdhsa_exception_fp_ieee_overflow 0
		.amdhsa_exception_fp_ieee_underflow 0
		.amdhsa_exception_fp_ieee_inexact 0
		.amdhsa_exception_int_div_zero 0
	.end_amdhsa_kernel

.LBB2_11:
	v_and_b32_e32 v28, 8, v0
	v_lshlrev_b32_e32 v34, 4, v0
	v_lshlrev_b32_e32 v0, 1, v5
	v_lshl_or_b32 v38, v6, 4, v0
	v_lshlrev_b32_e32 v0, 7, v1
	v_mov_b32_e32 v29, 0xeeeeeeee
	v_mov_b32_e32 v30, 0x44444444
	v_cmp_eq_u32_e32 vcc, 0, v28
	v_lshl_add_u64 v[2:3], s[20:21], 0, v[2:3]
	v_lshl_or_b32 v40, s24, 9, v0
	v_cndmask_b32_e64 v0, 0, 1, s[0:1]
	v_cndmask_b32_e32 v28, v29, v30, vcc
	s_waitcnt vmcnt(9)
	v_and_b32_e32 v44, 0xffff, v8
	s_waitcnt vmcnt(8)
	v_and_b32_e32 v43, 0xffff, v9
	s_waitcnt vmcnt(7)
	v_and_b32_e32 v42, 0xffff, v11
	s_waitcnt vmcnt(3)
	v_and_b32_e32 v41, 0xffff, v24
	v_and_b32_e32 v29, 0xffff, v10
	v_and_b32_e32 v30, 0xffff, v12
	s_waitcnt vmcnt(2)
	v_and_b32_e32 v31, 0xffff, v13
	s_waitcnt vmcnt(1)
	v_and_b32_e32 v32, 0xffff, v15
	v_and_b32_e32 v45, 0xffff, v14
	s_waitcnt vmcnt(0)
	v_and_b32_e32 v33, 0xffff, v25
	s_mov_b32 s19, 0x20000
	s_mov_b32 s18, 0x40000
	s_and_b32 s17, s9, 0xffff
	s_mov_b32 s16, s8
	v_lshl_add_u64 v[24:25], v[16:17], 2, v[2:3]
	v_lshlrev_b32_e32 v35, 9, v4
	v_lshlrev_b32_e32 v36, 7, v7
	v_lshlrev_b32_e32 v37, 4, v5
	v_cmp_eq_u32_e64 s[2:3], 0, v4
	v_lshl_or_b32 v39, v27, 14, v34
	s_mov_b64 s[6:7], 0
	s_mov_b32 s28, 0x10000
	v_cmp_ne_u32_e64 s[0:1], 1, v0
	v_mov_b32_e32 v46, 0
	s_mov_b32 s29, 0
	v_lshl_add_u32 v120, v27, 14, v40
	v_or_b32_e32 v120, v120, v38
	s_mov_b32 s37, 0
	s_cmp_eq_u32 s29, 0
	s_cbranch_scc1 .LBB2_23
.LBB2_12:
	s_add_i32 s12, s29, -1
	s_and_b32 s30, s12, 1
	s_bitcmp1_b32 s12, 1
	s_cselect_b32 s4, 0x10001, 0
	v_lshl_add_u32 v47, s30, 17, v39
	s_lshl_b32 s31, s30, 14
	s_lshl_b64 s[10:11], s[12:13], 12
	v_add_u32_e32 v48, 0x1000, v47
	v_add_u32_e32 v49, 0x2000, v47
	v_add_u32_e32 v50, 0x3000, v47
	v_or_b32_e32 v110, s31, v34
	v_add_u32_e32 v111, s31, v35
	v_lshl_add_u64 v[112:113], v[24:25], 0, s[10:11]
	v_add3_u32 v111, v111, v36, v37
	s_lshl_b32 s32, s29, 13
	s_add_i32 s32, s32, 0x2000
	s_mov_b32 s33, 0
	v_lshl_add_u64 v[114:115], v[20:21], 0, s[32:33]
	v_lshl_add_u64 v[118:119], v[22:23], 0, s[32:33]
	v_add_co_u32_e32 v116, vcc, 0x1000, v114
	v_mov_b64_e32 v[62:63], 0
	v_mov_b64_e32 v[64:65], 0
	v_addc_co_u32_e32 v117, vcc, 0, v115, vcc
	v_mov_b64_e32 v[66:67], 0
	v_mov_b64_e32 v[68:69], 0
	v_mov_b64_e32 v[70:71], 0
	v_mov_b64_e32 v[72:73], 0
	v_mov_b64_e32 v[74:75], 0
	v_mov_b64_e32 v[76:77], 0
	s_mov_b32 s31, 0
	s_sleep 1
.Lrec_poll:
	buffer_load_dwordx4 v[0:3], v47, s[16:19], 0 offen sc1
	buffer_load_dwordx4 v[4:7], v48, s[16:19], 0 offen sc1
	buffer_load_dwordx4 v[8:11], v49, s[16:19], 0 offen sc1
	buffer_load_dwordx4 v[12:15], v50, s[16:19], 0 offen sc1
	s_cmp_eq_u32 s4, 0
	s_cbranch_scc1 .Lrec_poll_or
	s_waitcnt vmcnt(3)
	v_and_b32_e32 v52, v0, v1
	v_bitop3_b32 v52, v52, v3, v2 bitop3:0x80
	s_waitcnt vmcnt(2)
	v_bitop3_b32 v52, v4, v5, v52 bitop3:0x80
	v_bitop3_b32 v52, v52, v7, v6 bitop3:0x80
	s_waitcnt vmcnt(1)
	v_bitop3_b32 v52, v8, v9, v52 bitop3:0x80
	v_bitop3_b32 v52, v52, v11, v10 bitop3:0x80
	s_waitcnt vmcnt(0)
	v_bitop3_b32 v52, v12, v13, v52 bitop3:0x80
	v_bitop3_b32 v52, v52, v15, v14 bitop3:0x80
	s_branch .Lrec_poll_chk
.Lrec_poll_or:
	s_waitcnt vmcnt(3)
	v_or_b32_e32 v52, v0, v1
	v_or3_b32 v52, v52, v2, v3
	s_waitcnt vmcnt(2)
	v_or3_b32 v52, v4, v52, v5
	v_or3_b32 v52, v52, v6, v7
	s_waitcnt vmcnt(1)
	v_or3_b32 v52, v8, v52, v9
	v_or3_b32 v52, v52, v10, v11
	s_waitcnt vmcnt(0)
	v_or3_b32 v52, v12, v52, v13
	v_or3_b32 v52, v52, v14, v15
.Lrec_poll_chk:
	v_and_b32_e32 v52, 0x10001, v52
	v_cmp_eq_u32_e32 vcc, s4, v52
	s_andn2_b64 exec, exec, vcc
	s_cbranch_execz .LBB2_20
	s_add_i32 s31, s31, 1
	s_cmp_lg_u32 s6, 0
	s_cbranch_scc1 .Lrec_dead
	s_cmp_le_u32 s31, 0x10000
	s_cbranch_scc1 .Lrec_poll
.Lrec_dead:
	s_mov_b32 s6, 1
.LBB2_20:
	s_mov_b64 exec, -1
	s_waitcnt vmcnt(3)
	ds_write_b128 v110, v[0:3]
	s_waitcnt vmcnt(2)
	ds_write_b128 v110, v[4:7] offset:4096
	s_waitcnt vmcnt(1)
	ds_write_b128 v110, v[8:11] offset:8192
	s_waitcnt vmcnt(0)
	ds_write_b128 v110, v[12:15] offset:12288
	s_cmpk_eq_i32 s29, 0x7f
	s_waitcnt lgkmcnt(0)
	s_barrier
	ds_read_b128 v[0:3], v111
	ds_read_b128 v[4:7], v111 offset:1024
	ds_read_b128 v[8:11], v111 offset:2048
	ds_read_b128 v[12:15], v111 offset:3072
	global_store_dword v[112:113], v46, off
	ds_read_b128 v[46:49], v111 offset:4096
	ds_read_b128 v[50:53], v111 offset:5120
	ds_read_b128 v[54:57], v111 offset:6144
	ds_read_b128 v[58:61], v111 offset:7168
	ds_read_b128 v[78:81], v111 offset:14336
	ds_read_b128 v[82:85], v111 offset:15360
	ds_read_b128 v[86:89], v111 offset:8192
	ds_read_b128 v[90:93], v111 offset:9216
	ds_read_b128 v[94:97], v111 offset:10240
	ds_read_b128 v[98:101], v111 offset:11264
	ds_read_b128 v[102:105], v111 offset:12288
	ds_read_b128 v[106:109], v111 offset:13312
	s_cbranch_scc1 .Lrec_nopf
	global_load_ushort v29, v[114:115], off
	global_load_ushort v30, v[114:115], off offset:2048
	global_load_ushort v31, v[116:117], off
	global_load_ushort v32, v[116:117], off offset:2048
	global_load_ushort v33, v[118:119], off
.Lrec_nopf:
	v_cvt_f32_f16_e32 v112, v44
	v_cvt_f32_f16_e32 v113, v43
	v_cvt_f32_f16_e32 v114, v42
	v_cvt_f32_f16_e32 v115, v41
	v_cvt_f32_f16_e32 v118, v45
	v_cndmask_b32_e64 v116, 0, v118, s[22:23]
	v_cndmask_b32_e64 v117, v118, 0, s[22:23]
	s_waitcnt lgkmcnt(14)
	v_smfmac_f32_16x16x64_f16 v[62:65], v[0:3], a[0:7], v28
	v_smfmac_f32_16x16x64_f16 v[66:69], v[0:3], a[128:135], v28
	v_smfmac_f32_16x16x64_f16 v[70:73], v[4:7], a[8:15], v28
	v_smfmac_f32_16x16x64_f16 v[74:77], v[4:7], a[136:143], v28
	s_waitcnt lgkmcnt(13)
	v_smfmac_f32_16x16x64_f16 v[62:65], v[8:11], a[16:23], v28
	v_smfmac_f32_16x16x64_f16 v[66:69], v[8:11], a[144:151], v28
	s_waitcnt lgkmcnt(12)
	v_smfmac_f32_16x16x64_f16 v[70:73], v[12:15], a[24:31], v28
	v_smfmac_f32_16x16x64_f16 v[74:77], v[12:15], a[152:159], v28
	s_waitcnt lgkmcnt(11)
	v_smfmac_f32_16x16x64_f16 v[62:65], v[46:49], a[32:39], v28
	v_smfmac_f32_16x16x64_f16 v[66:69], v[46:49], a[160:167], v28
	s_waitcnt lgkmcnt(10)
	v_smfmac_f32_16x16x64_f16 v[70:73], v[50:53], a[40:47], v28
	v_smfmac_f32_16x16x64_f16 v[74:77], v[50:53], a[168:175], v28
	s_waitcnt lgkmcnt(9)
	v_smfmac_f32_16x16x64_f16 v[62:65], v[54:57], a[48:55], v28
	v_smfmac_f32_16x16x64_f16 v[66:69], v[54:57], a[176:183], v28
	s_waitcnt lgkmcnt(8)
	v_smfmac_f32_16x16x64_f16 v[70:73], v[58:61], a[56:63], v28
	v_smfmac_f32_16x16x64_f16 v[74:77], v[58:61], a[184:191], v28
	s_waitcnt lgkmcnt(5)
	v_smfmac_f32_16x16x64_f16 v[62:65], v[86:89], a[64:71], v28
	v_smfmac_f32_16x16x64_f16 v[66:69], v[86:89], a[192:199], v28
	s_waitcnt lgkmcnt(4)
	v_smfmac_f32_16x16x64_f16 v[70:73], v[90:93], a[72:79], v28
	v_smfmac_f32_16x16x64_f16 v[74:77], v[90:93], a[200:207], v28
	s_waitcnt lgkmcnt(3)
	v_smfmac_f32_16x16x64_f16 v[62:65], v[94:97], a[80:87], v28
	v_smfmac_f32_16x16x64_f16 v[66:69], v[94:97], a[208:215], v28
	s_waitcnt lgkmcnt(2)
	v_smfmac_f32_16x16x64_f16 v[70:73], v[98:101], a[88:95], v28
	v_smfmac_f32_16x16x64_f16 v[74:77], v[98:101], a[216:223], v28
	s_waitcnt lgkmcnt(1)
	v_smfmac_f32_16x16x64_f16 v[62:65], v[102:105], a[96:103], v28
	v_smfmac_f32_16x16x64_f16 v[66:69], v[102:105], a[224:231], v28
	s_waitcnt lgkmcnt(0)
	v_smfmac_f32_16x16x64_f16 v[70:73], v[106:109], a[104:111], v28
	v_smfmac_f32_16x16x64_f16 v[74:77], v[106:109], a[232:239], v28
	v_smfmac_f32_16x16x64_f16 v[62:65], v[78:81], a[112:119], v28
	v_smfmac_f32_16x16x64_f16 v[66:69], v[78:81], a[240:247], v28
	v_smfmac_f32_16x16x64_f16 v[70:73], v[82:85], a[120:127], v28
	v_smfmac_f32_16x16x64_f16 v[74:77], v[82:85], a[248:255], v28
	s_nop 6
	v_add_f32_e64 v0, v72, v64
	v_add_f32_e64 v1, v73, v65
	v_pk_add_f32 v[2:3], v[70:71], v[62:63]
	v_pk_add_f32 v[4:5], v[76:77], v[68:69]
	v_pk_add_f32 v[6:7], v[74:75], v[66:67]
	s_waitcnt vmcnt(0)
	s_branch .LBB2_24
.LBB2_23:
	v_mov_b32_e32 v1, 0
	v_mov_b32_e32 v0, v1
	v_mov_b32_e32 v3, v1
	v_mov_b32_e32 v2, v1
	v_mov_b32_e32 v5, v1
	v_mov_b32_e32 v4, v1
	v_mov_b32_e32 v7, v1
	v_mov_b32_e32 v6, v1
	v_cvt_f32_f16_e32 v112, v44
	v_cvt_f32_f16_e32 v113, v43
	v_cvt_f32_f16_e32 v114, v42
	v_cvt_f32_f16_e32 v115, v41
	v_cvt_f32_f16_e32 v118, v45
	v_cndmask_b32_e64 v116, 0, v118, s[22:23]
	v_cndmask_b32_e64 v117, v118, 0, s[22:23]
.LBB2_24:
	v_permlane32_swap_b32_e32 v2, v3
	v_permlane32_swap_b32_e32 v0, v1
	v_permlane32_swap_b32_e32 v6, v7
	v_permlane32_swap_b32_e32 v4, v5
	v_add_f32_e32 v2, v2, v3
	v_add_f32_e32 v0, v0, v1
	v_add_f32_e32 v1, v6, v7
	v_add_f32_e32 v3, v4, v5
	v_cndmask_b32_e64 v4, v2, v0, s[2:3]
	v_mov_b32_e32 v6, 0
	v_cndmask_b32_e64 v5, v1, v3, s[2:3]
	v_mov_b32_e32 v7, 0
	v_mov_b32_dpp v6, v4 row_ror:8 row_mask:0xf bank_mask:0xf
	s_nop 0
	v_mov_b32_dpp v7, v5 row_ror:8 row_mask:0xf bank_mask:0xf
	v_cndmask_b32_e64 v0, v0, v6, s[2:3]
	v_cndmask_b32_e64 v2, v6, v2, s[2:3]
	v_cndmask_b32_e64 v1, v7, v1, s[2:3]
	v_cndmask_b32_e64 v3, v3, v7, s[2:3]
	v_add_f32_e32 v2, v2, v112
	v_add_f32_e32 v0, v0, v113
	v_add_f32_e32 v1, v1, v114
	v_add_f32_e32 v3, v3, v115
	v_add_f32_e32 v0, v116, v0
	v_add_f32_e32 v3, v117, v3
	v_mul_f32_e32 v2, 0xbfb8aa3b, v2
	v_mul_f32_e32 v1, 0x4038aa3b, v1
	v_mul_f32_e32 v0, 0xbfb8aa3b, v0
	v_exp_f32_e32 v1, v1
	v_exp_f32_e32 v2, v2
	v_exp_f32_e32 v0, v0
	v_mul_f32_e32 v3, 0xbfb8aa3b, v3
	v_add_f32_e32 v1, 1.0, v1
	v_add_f32_e32 v2, 1.0, v2
	v_exp_f32_e32 v3, v3
	v_rcp_f32_e32 v1, v1
	v_add_f32_e32 v0, 1.0, v0
	v_rcp_f32_e32 v2, v2
	v_rcp_f32_e32 v5, v0
	v_add_f32_e32 v3, 1.0, v3
	v_fma_f32 v0, v1, -2.0, 1.0
	v_mul_f32_e32 v0, v2, v0
	v_rcp_f32_e32 v3, v3
	v_fmac_f32_e32 v0, v26, v5
	v_mul_f32_e32 v1, 0x4038aa3b, v0
	v_exp_f32_e32 v1, v1
	s_cmpk_eq_i32 s29, 0x7f
	s_nop 0
	v_add_f32_e32 v1, 1.0, v1
	v_rcp_f32_e32 v1, v1
	s_nop 0
	v_fma_f32 v1, v1, -2.0, 1.0
	v_mul_f32_e32 v46, v3, v1
	s_cbranch_scc1 .LBB2_29
	v_cvt_f16_f32_e32 v2, v46
	s_cmp_lg_u64 s[0:1], 0
	v_bitop3_b16 v2, s37, v2, -2 bitop3:0xf8
	s_cbranch_scc1 .Lrec_pub_slow
	global_store_short v120, v2, s[8:9]
	s_branch .LBB2_29
.Lrec_pub_slow:
	buffer_store_short v2, v120, s[16:19], 0 offen sc1
.LBB2_29:
	s_add_i32 s29, s29, 1
	s_cmpk_eq_i32 s29, 0x80
	s_cbranch_scc1 .LBB2_31
	v_mov_b32_e32 v44, v29
	v_mov_b32_e32 v43, v30
	v_mov_b32_e32 v42, v31
	v_mov_b32_e32 v41, v32
	v_mov_b32_e32 v45, v33
	v_mov_b32_e32 v26, v0
	s_lshl_b32 s4, s29, 3
	s_and_b32 s4, s4, 8
	s_bfe_u32 s37, s29, 0x10001
	v_add_u32_e32 v120, s4, v27
	v_lshl_add_u32 v120, v120, 14, v40
	v_or_b32_e32 v120, v120, v38
	s_branch .LBB2_12

	.amdhsa_kernel _Z8lstm_recPK15HIP_vector_typeIjLj4EEPKtS4_PjS5_Pf
		.amdhsa_group_segment_fixed_size 32780
		.amdhsa_private_segment_fixed_size 0
		.amdhsa_kernarg_size 48
		.amdhsa_user_sgpr_count 2
		.amdhsa_user_sgpr_dispatch_ptr 0
		.amdhsa_user_sgpr_queue_ptr 0
		.amdhsa_user_sgpr_kernarg_segment_ptr 1
		.amdhsa_user_sgpr_dispatch_id 0
		.amdhsa_user_sgpr_kernarg_preload_length 0
		.amdhsa_user_sgpr_kernarg_preload_offset 0
		.amdhsa_user_sgpr_private_segment_size 0
		.amdhsa_uses_dynamic_stack 0
		.amdhsa_enable_private_segment 0
		.amdhsa_system_sgpr_workgroup_id_x 1
		.amdhsa_system_sgpr_workgroup_id_y 0
		.amdhsa_system_sgpr_workgroup_id_z 0
		.amdhsa_system_sgpr_workgroup_info 0
		.amdhsa_system_vgpr_workitem_id 0
		.amdhsa_next_free_vgpr 384
		.amdhsa_next_free_sgpr 96
		.amdhsa_accum_offset 128
		.amdhsa_reserve_vcc 1
		.amdhsa_float_round_mode_32 0
		.amdhsa_float_round_mode_16_64 0
		.amdhsa_float_denorm_mode_32 3
		.amdhsa_float_denorm_mode_16_64 3
		.amdhsa_dx10_clamp 1
		.amdhsa_ieee_mode 1
		.amdhsa_fp16_overflow 0
		.amdhsa_tg_split 0
		.amdhsa_exception_fp_ieee_invalid_op 0
		.amdhsa_exception_fp_denorm_src 0
		.amdhsa_exception_fp_ieee_div_zero 0
		.amdhsa_exception_fp_ieee_overflow 0
		.amdhsa_exception_fp_ieee_underflow 0
		.amdhsa_exception_fp_ieee_inexact 0
		.amdhsa_exception_int_div_zero 0
	.end_amdhsa_kernel

amdhsa.kernels:
  - .agpr_count:     0
    .args:
      - .actual_access:  read_only
        .address_space:  global
        .offset:         0
        .size:           8
        .value_kind:     global_buffer
      - .actual_access:  read_only
        .address_space:  global
        .offset:         8
        .size:           8
        .value_kind:     global_buffer
      - .actual_access:  read_only
        .address_space:  global
        .offset:         16
        .size:           8
        .value_kind:     global_buffer
      - .actual_access:  read_only
        .address_space:  global
        .offset:         24
        .size:           8
        .value_kind:     global_buffer
      - .actual_access:  read_only
        .address_space:  global
        .offset:         32
        .size:           8
        .value_kind:     global_buffer
      - .actual_access:  read_only
        .address_space:  global
        .offset:         40
        .size:           8
        .value_kind:     global_buffer
      - .actual_access:  read_only
        .address_space:  global
        .offset:         48
        .size:           8
        .value_kind:     global_buffer
      - .actual_access:  read_only
        .address_space:  global
        .offset:         56
        .size:           8
        .value_kind:     global_buffer
      - .actual_access:  read_only
        .address_space:  global
        .offset:         64
        .size:           8
        .value_kind:     global_buffer
      - .actual_access:  read_only
        .address_space:  global
        .offset:         72
        .size:           8
        .value_kind:     global_buffer
      - .actual_access:  read_only
        .address_space:  global
        .offset:         80
        .size:           8
        .value_kind:     global_buffer
      - .actual_access:  write_only
        .address_space:  global
        .offset:         88
        .size:           8
        .value_kind:     global_buffer
      - .actual_access:  write_only
        .address_space:  global
        .offset:         96
        .size:           8
        .value_kind:     global_buffer
      - .actual_access:  write_only
        .address_space:  global
        .offset:         104
        .size:           8
        .value_kind:     global_buffer
      - .actual_access:  write_only
        .address_space:  global
        .offset:         112
        .size:           8
        .value_kind:     global_buffer
      - .actual_access:  write_only
        .address_space:  global
        .offset:         120
        .size:           8
        .value_kind:     global_buffer
    .group_segment_fixed_size: 0
    .kernarg_segment_align: 8
    .kernarg_segment_size: 128
    .language:       OpenCL C
    .language_version:
      - 2
      - 0
    .max_flat_workgroup_size: 256
    .name:           _Z8pack_allPKfS0_S0_S0_S0_S0_S0_S0_S0_S0_S0_P15HIP_vector_typeIjLj4EES3_PfS3_Pj
    .private_segment_fixed_size: 0
    .sgpr_count:     28
    .sgpr_spill_count: 0
    .symbol:         _Z8pack_allPKfS0_S0_S0_S0_S0_S0_S0_S0_S0_S0_P15HIP_vector_typeIjLj4EES3_PfS3_Pj.kd
    .uniform_work_group_size: 1
    .uses_dynamic_stack: false
    .vgpr_count:     24
    .vgpr_spill_count: 0
    .wavefront_size: 64
  - .agpr_count:     0
    .args:
      - .address_space:  global
        .offset:         0
        .size:           8
        .value_kind:     global_buffer
      - .address_space:  global
        .offset:         8
        .size:           8
        .value_kind:     global_buffer
      - .actual_access:  read_only
        .address_space:  global
        .offset:         16
        .size:           8
        .value_kind:     global_buffer
      - .actual_access:  write_only
        .address_space:  global
        .offset:         24
        .size:           8
        .value_kind:     global_buffer
      - .actual_access:  write_only
        .address_space:  global
        .offset:         32
        .size:           8
        .value_kind:     global_buffer
    .group_segment_fixed_size: 0
    .kernarg_segment_align: 8
    .kernarg_segment_size: 40
    .language:       OpenCL C
    .language_version:
      - 2
      - 0
    .max_flat_workgroup_size: 512
    .name:           _Z7gemm_gxPKtS0_PKfPtS3_
    .private_segment_fixed_size: 0
    .sgpr_count:     58
    .sgpr_spill_count: 0
    .symbol:         _Z7gemm_gxPKtS0_PKfPtS3_.kd
    .uniform_work_group_size: 1
    .uses_dynamic_stack: false
    .vgpr_count:     256
    .vgpr_spill_count: 0
    .wavefront_size: 64
  - .agpr_count:     256
    .args:
      - .actual_access:  read_only
        .address_space:  global
        .offset:         0
        .size:           8
        .value_kind:     global_buffer
      - .actual_access:  read_only
        .address_space:  global
        .offset:         8
        .size:           8
        .value_kind:     global_buffer
      - .actual_access:  read_only
        .address_space:  global
        .offset:         16
        .size:           8
        .value_kind:     global_buffer
      - .address_space:  global
        .offset:         24
        .size:           8
        .value_kind:     global_buffer
      - .address_space:  global
        .offset:         32
        .size:           8
        .value_kind:     global_buffer
      - .actual_access:  write_only
        .address_space:  global
        .offset:         40
        .size:           8
        .value_kind:     global_buffer
    .group_segment_fixed_size: 32780
    .kernarg_segment_align: 8
    .kernarg_segment_size: 48
    .language:       OpenCL C
    .language_version:
      - 2
      - 0
    .max_flat_workgroup_size: 256
    .name:           _Z8lstm_recPK15HIP_vector_typeIjLj4EEPKtS4_PjS5_Pf
    .private_segment_fixed_size: 0
    .sgpr_count:     42
    .sgpr_spill_count: 0
    .symbol:         _Z8lstm_recPK15HIP_vector_typeIjLj4EEPKtS4_PjS5_Pf.kd
    .uniform_work_group_size: 1
    .uses_dynamic_stack: false
    .vgpr_count:     384
    .vgpr_spill_count: 0
    .wavefront_size: 64
